# s16p + cross-row reductions via v_permlane16/32_swap (norm1 L0 keep/send steps, wave sums, attention softmax row max, GEMM row-ss partials); without the phase-0/lambda hoists; padded
# speedup vs baseline: 1.0048x; 1.0048x over previous
.LBB0_1115:
	s_cmp_lt_u32 s3, 0x40001
	s_mov_b64 s[18:19], 0
	s_cselect_b64 s[20:21], -1, 0
	s_mov_b64 s[22:23], -1
	s_and_b64 vcc, exec, s[20:21]
	s_cbranch_vccnz .LBB0_1112
	s_branch .LBB0_1109
	s_nop 0
	s_nop 0
	s_nop 0
	s_nop 0
	s_nop 0
	s_nop 0
	s_nop 0
	s_nop 0
	s_nop 0
	s_nop 0
	s_nop 0
	s_nop 0
	s_nop 0
	s_nop 0
	s_nop 0
	s_nop 0
	s_nop 0
	s_nop 0
	s_nop 0
	s_nop 0
	s_nop 0
	s_nop 0
	s_nop 0
	s_nop 0
	s_nop 0
	s_nop 0
	s_nop 0
	s_nop 0
	s_nop 0
	s_nop 0
	s_nop 0
	s_nop 0
	s_nop 0
	s_nop 0
	s_nop 0
	s_nop 0
	s_nop 0
	s_nop 0
	s_nop 0
	s_nop 0
	s_nop 0
	s_nop 0
	s_nop 0
	s_nop 0
	s_nop 0
	s_nop 0
	s_nop 0
	s_nop 0
	s_nop 0
	s_nop 0
	s_nop 0
	s_nop 0
	s_nop 0
	s_nop 0
	s_nop 0
	s_nop 0
	s_nop 0
	s_nop 0
	s_nop 0
	s_nop 0
	s_nop 0
	s_nop 0
	s_nop 0
